# final RMSNorm phase rewritten by hand: g_final hoisted to registers, 2 rows of loads in flight per wave (software pipeline)
# speedup vs baseline: 1.0055x; 1.0055x over previous
.LBB0_336:
	s_or_b64 exec, exec, s[2:3]
	s_and_b32 s1, s0, 0x3fffffc0
	s_ashr_i32 s2, s0, 8
	s_ashr_i32 s0, s0, 5
	s_and_b32 s21, s0, -2
	s_lshl_b32 s0, s2, 7
	s_add_i32 s0, s0, 0
	v_and_b32_e32 v3, 63, v18
	v_and_b32_e32 v82, 31, v18
	s_add_i32 s0, s0, 0x10000
	v_lshlrev_b32_e32 v5, 4, v18
	v_bfe_u32 v4, v18, 5, 1
	v_and_b32_e32 v6, 0x70, v5
	v_lshl_add_u32 v89, v82, 8, s0
	s_add_i32 s0, 0, 0x20200
	v_lshlrev_b32_e32 v8, 2, v82
	v_cmp_gt_u32_e64 s[40:41], 32, v3
	v_lshlrev_b32_e32 v3, 3, v3
	v_and_b32_e32 v5, 0xc0, v5
	v_lshlrev_b32_e32 v11, 1, v18
	v_lshlrev_b32_e32 v7, 4, v4
	v_add_u32_e32 v91, s0, v8
	v_readlane_b32 s0, v253, 36
	v_and_b32_e32 v10, 24, v3
	v_and_b32_e32 v11, 32, v11
	v_add_u32_e32 v5, 0, v5
	s_lshl_b32 s1, s1, 2
	v_add_u32_e32 v93, s0, v7
	v_or_b32_e32 v9, 0x80, v82
	v_and_b32_e32 v3, 0x100, v3
	s_lshl_b32 s0, s2, 10
	v_add3_u32 v5, v5, v10, v11
	s_add_i32 s1, s1, 0
	v_bitop3_b32 v87, v7, v6, 32 bitop3:0x36
	v_add3_u32 v95, v5, v3, s0
	v_readlane_b32 s2, v251, 25
	v_and_b32_e32 v3, 3, v18
	v_bitop3_b32 v97, v7, v6, 64 bitop3:0x36
	v_bitop3_b32 v99, v7, v6, s94 bitop3:0x36
	v_mad_i32_i24 v6, v4, -4, v9
	s_movk_i32 s0, 0x80
	s_add_i32 s1, s1, 0x22900
	v_mov_b32_e32 v83, v203
	v_readlane_b32 s3, v251, 26
	v_cmp_eq_u32_e64 s[42:43], 0, v3
	v_mad_i32_i24 v3, v4, -4, -1
	v_cmp_gt_u32_e64 s[46:47], s0, v6
	v_mad_i32_i24 v6, v4, -4, -2
	v_lshl_add_u64 v[84:85], s[2:3], 0, v[82:83]
	v_add_u32_e32 v83, s1, v8
	v_add_u32_e32 v5, v3, v9
	v_add_u32_e32 v8, v6, v9
	v_cmp_gt_u32_e64 s[44:45], s0, v5
	v_mad_i32_i24 v5, v4, -4, -3
	v_cmp_gt_u32_e64 s[50:51], s0, v8
	v_mad_i32_i24 v8, v4, -4, -9
	v_add_u32_e32 v10, v5, v9
	v_add_u32_e32 v12, v8, v9
	v_cmp_gt_u32_e64 s[48:49], s0, v10
	v_mad_i32_i24 v10, v4, -4, -8
	v_cmp_gt_u32_e64 s[52:53], s0, v12
	v_mad_i32_i24 v12, v4, -4, -10
	v_add_u32_e32 v3, v3, v82
	v_add_u32_e32 v11, v10, v9
	v_add_u32_e32 v13, v12, v9
	v_cmp_lt_i32_e64 s[78:79], -1, v3
	v_add_u32_e32 v3, v6, v82
	v_cmp_gt_u32_e64 s[54:55], s0, v11
	v_mad_i32_i24 v11, v4, -4, -11
	v_cmp_gt_u32_e64 s[58:59], s0, v13
	v_not_b32_e32 v13, 16
	v_cmp_lt_i32_e64 s[80:81], -1, v3
	v_add_u32_e32 v3, v5, v82
	v_add_u32_e32 v14, v11, v9
	v_mad_i32_i24 v13, v4, -4, v13
	v_cmp_lt_i32_e64 s[82:83], -1, v3
	v_add_u32_e32 v3, v10, v82
	v_cmp_gt_u32_e64 s[56:57], s0, v14
	v_mad_i32_i24 v14, v4, -4, -16
	v_add_u32_e32 v16, v13, v9
	v_cmp_lt_i32_e64 s[84:85], -1, v3
	v_add_u32_e32 v3, v8, v82
	v_add_u32_e32 v15, v14, v9
	v_cmp_gt_u32_e64 s[60:61], s0, v16
	v_not_b32_e32 v16, 17
	v_cmp_lt_i32_e64 s[86:87], -1, v3
	v_add_u32_e32 v3, v12, v82
	v_cmp_gt_u32_e64 s[62:63], s0, v15
	v_not_b32_e32 v15, 18
	v_mad_i32_i24 v16, v4, -4, v16
	v_cmp_lt_i32_e64 s[88:89], -1, v3
	v_add_u32_e32 v3, v11, v82
	v_mad_i32_i24 v15, v4, -4, v15
	v_add_u32_e32 v17, v16, v9
	v_cmp_lt_i32_e64 s[90:91], -1, v3
	v_add_u32_e32 v3, v14, v82
	v_bitop3_b32 v1, v4, v18, 7 bitop3:0x78
	v_add_u32_e32 v18, v15, v9
	v_cmp_gt_u32_e64 s[66:67], s0, v17
	v_not_b32_e32 v17, 24
	v_cmp_lt_i32_e64 s[92:93], -1, v3
	v_add_u32_e32 v3, v13, v82
	v_cmp_gt_u32_e64 s[64:65], s0, v18
	v_mad_i32_i24 v17, v4, -4, v17
	v_not_b32_e32 v18, 23
	v_cmp_lt_i32_e64 s[94:95], -1, v3
	v_add_u32_e32 v3, v16, v82
	v_mad_i32_i24 v18, v4, -4, v18
	v_add_u32_e32 v20, v17, v9
	v_cmp_lt_i32_e64 s[96:97], -1, v3
	v_add_u32_e32 v3, v15, v82
	v_add_u32_e32 v19, v18, v9
	v_cmp_gt_u32_e64 s[68:69], s0, v20
	v_not_b32_e32 v20, 25
	v_cmp_lt_i32_e64 s[4:5], -1, v3
	v_add_u32_e32 v3, v18, v82
	v_cmp_gt_u32_e64 s[70:71], s0, v19
	v_not_b32_e32 v19, 26
	v_mad_i32_i24 v20, v4, -4, v20
	v_cmp_lt_i32_e64 s[2:3], -1, v3
	v_add_u32_e32 v3, v17, v82
	v_mad_i32_i24 v19, v4, -4, v19
	v_cmp_lt_i32_e64 s[6:7], -1, v3
	v_add_u32_e32 v3, v20, v82
	v_lshlrev_b32_e32 v2, 3, v4
	v_lshlrev_b32_e32 v86, 2, v4
	v_add_u32_e32 v21, v20, v9
	v_add_u32_e32 v9, v19, v9
	v_mad_i32_i24 v4, v4, -4, v82
	v_cmp_lt_i32_e64 s[8:9], -1, v3
	v_add_u32_e32 v3, v19, v82
	v_lshlrev_b32_e32 v1, 4, v1
	s_mov_b32 s16, 0
	v_cmp_gt_u32_e64 s[72:73], s0, v9
	v_cmp_gt_u32_e64 s[74:75], s0, v21
	v_cmp_lt_i32_e64 s[76:77], -1, v4
	v_cmp_lt_i32_e64 s[10:11], -1, v3
	v_add_u32_e32 v101, s1, v7
	v_or_b32_e32 v88, 1, v86
	v_or_b32_e32 v90, 2, v86
	v_or_b32_e32 v92, 3, v86
	v_or_b32_e32 v94, 8, v86
	v_or_b32_e32 v96, 9, v86
	v_or_b32_e32 v98, 10, v86
	v_or_b32_e32 v100, 11, v86
	v_or_b32_e32 v102, 16, v86
	v_or_b32_e32 v104, 17, v86
	v_or_b32_e32 v106, 18, v86
	v_or_b32_e32 v108, 19, v86
	v_or_b32_e32 v110, 24, v86
	v_or_b32_e32 v112, 25, v86
	v_or_b32_e32 v114, 26, v86
	v_or_b32_e32 v116, 27, v86
	v_lshlrev_b32_e32 v202, 1, v2
	s_waitcnt lgkmcnt(0)
	s_barrier
	s_branch .LBB0_338

.LBB0_338:
	s_lshr_b32 s0, s16, 2
	s_or_b32 vcc_lo, s0, s21
	s_and_b32 s0, s16, 3
	s_lshl_b32 s1, s0, 5
	s_or_b32 s17, s26, s1
	v_mov_b32_e32 v3, s27
	v_or_b32_e32 v2, s17, v82
	v_readlane_b32 s18, v250, 9
	v_lshlrev_b64 v[2:3], 11, v[2:3]
	v_readlane_b32 s19, v250, 10
	s_lshl_b32 s22, vcc_lo, 6
	s_ashr_i32 s23, s22, 31
	v_lshl_add_u64 v[2:3], s[18:19], 0, v[2:3]
	v_lshl_add_u64 v[2:3], s[22:23], 1, v[2:3]
	v_lshl_add_u64 v[118:119], v[2:3], 0, v[202:203]
	global_load_dwordx4 v[2:5], v[118:119], off
	s_lshl_b32 s19, s0, 13
	v_add_u32_e32 v103, s19, v89
	v_add_u32_e32 v18, v103, v1
	ds_read_b128 v[6:9], v18
	ds_read_b128 v[10:13], v18 offset:32768
	v_add_u32_e32 v105, v103, v87
	s_ashr_i32 vcc_hi, vcc_lo, 31
	s_lshl_b64 s[28:29], vcc, 2
	s_add_u32 s28, s24, s28
	s_addc_u32 s29, s37, s29
	s_mul_i32 s1, vcc_lo, 0x210
	s_add_i32 s1, s1, 0
	s_mov_b32 s18, s27
	s_add_i32 s1, s1, 0x20800
	s_and_b64 vcc, exec, s[38:39]
	v_lshl_add_u32 v131, s0, 7, v93
	v_mov_b32_e32 v107, 0xff800000
	v_mov_b32_e32 v109, 0xff800000
	v_mov_b32_e32 v115, 0xff800000
	v_mov_b32_e32 v111, 0xff800000
	v_mov_b32_e32 v117, 0xff800000
	v_mov_b32_e32 v113, 0xff800000
	v_mov_b32_e32 v129, 0xff800000
	v_mov_b32_e32 v128, 0xff800000
	s_waitcnt vmcnt(0) lgkmcnt(1)
	v_mfma_f32_32x32x16_bf16 v[66:81], v[6:9], v[2:5], 0
	ds_read_b128 v[6:9], v18 offset:8192
	ds_read_b128 v[14:17], v18 offset:16384
	global_load_dwordx4 v[120:123], v[118:119], off offset:32
	ds_read_b128 v[124:127], v105 offset:32768
	s_waitcnt lgkmcnt(2)
	v_mfma_f32_32x32x16_bf16 v[50:65], v[6:9], v[2:5], 0
	ds_read_b128 v[6:9], v18 offset:24576
	s_waitcnt lgkmcnt(2)
	v_mfma_f32_32x32x16_bf16 v[34:49], v[14:17], v[2:5], 0
	s_waitcnt lgkmcnt(0)
	v_mfma_f32_32x32x16_bf16 v[18:33], v[6:9], v[2:5], 0
	ds_read_b128 v[6:9], v105
	ds_read_b128 v[14:17], v105 offset:8192
	global_load_dwordx4 v[132:135], v[118:119], off offset:64
	s_waitcnt vmcnt(1) lgkmcnt(1)
	v_mfma_f32_32x32x16_bf16 v[66:81], v[6:9], v[120:123], v[66:81]
	s_waitcnt lgkmcnt(0)
	v_mfma_f32_32x32x16_bf16 v[50:65], v[14:17], v[120:123], v[50:65]
	ds_read_b128 v[6:9], v105 offset:16384
	ds_read_b128 v[14:17], v105 offset:24576
	global_load_dwordx4 v[136:139], v[118:119], off offset:96
	v_add_u32_e32 v105, v103, v97
	v_add_u32_e32 v103, v103, v99
	v_mov_b32_e32 v118, 0xff800000
	s_waitcnt lgkmcnt(1)
	v_mfma_f32_32x32x16_bf16 v[34:49], v[6:9], v[120:123], v[34:49]
	ds_read_b128 v[6:9], v105
	ds_read_b128 v[140:143], v105 offset:32768
	s_waitcnt lgkmcnt(2)
	v_mfma_f32_32x32x16_bf16 v[18:33], v[14:17], v[120:123], v[18:33]
	s_waitcnt vmcnt(1) lgkmcnt(1)
	v_mfma_f32_32x32x16_bf16 v[66:81], v[6:9], v[132:135], v[66:81]
	ds_read_b128 v[6:9], v105 offset:8192
	ds_read_b128 v[14:17], v105 offset:16384
	s_waitcnt lgkmcnt(1)
	v_mfma_f32_32x32x16_bf16 v[50:65], v[6:9], v[132:135], v[50:65]
	s_waitcnt lgkmcnt(0)
	v_mfma_f32_32x32x16_bf16 v[34:49], v[14:17], v[132:135], v[34:49]
	ds_read_b128 v[6:9], v103
	ds_read_b128 v[14:17], v103 offset:8192
	s_waitcnt vmcnt(0) lgkmcnt(1)
	v_mfma_f32_32x32x16_bf16 v[66:81], v[6:9], v[136:139], v[66:81]
	s_waitcnt lgkmcnt(0)
	v_mfma_f32_32x32x16_bf16 v[50:65], v[14:17], v[136:139], v[50:65]
	ds_read_b128 v[6:9], v103 offset:16384
	ds_read_b128 v[14:17], v103 offset:24576
	s_waitcnt lgkmcnt(1)
	v_mfma_f32_32x32x16_bf16 v[34:49], v[6:9], v[136:139], v[34:49]
	ds_read_b128 v[6:9], v105 offset:24576
	ds_read_b128 v[144:147], v103 offset:32768
	global_load_dword v103, v203, s[28:29]
	s_waitcnt vmcnt(0)
	v_mov_b32_e32 v130, v103
	s_waitcnt lgkmcnt(1)
	v_mfma_f32_32x32x16_bf16 v[18:33], v[6:9], v[132:135], v[18:33]
	v_lshl_add_u32 v6, s0, 7, v91
	ds_read_b32 v105, v6
	v_mfma_f32_32x32x16_bf16 v[18:33], v[14:17], v[136:139], v[18:33]
	v_mfma_f32_32x32x16_bf16 v[2:17], v[10:13], v[2:5], 0
	v_mfma_f32_32x32x16_bf16 v[2:17], v[124:127], v[120:123], v[2:17]
	v_mov_b32_e32 v121, 0xff800000
	v_mov_b32_e32 v120, 0xff800000
	v_mov_b32_e32 v123, 0xff800000
	v_mov_b32_e32 v122, 0xff800000
	v_mov_b32_e32 v126, 0xff800000
	v_mov_b32_e32 v124, 0xff800000
	v_mov_b32_e32 v127, 0xff800000
	v_mfma_f32_32x32x16_bf16 v[2:17], v[140:143], v[132:135], v[2:17]
	v_mov_b32_e32 v125, 0xff800000
	s_waitcnt lgkmcnt(1)
	v_mfma_f32_32x32x16_bf16 v[2:17], v[144:147], v[136:139], v[2:17]
	s_cbranch_vccnz .LBB0_340
	ds_read_b128 v[120:123], v131
	ds_read_b128 v[124:127], v131 offset:32
	s_waitcnt lgkmcnt(1)
	v_sub_u32_e32 v107, v105, v120
	s_waitcnt lgkmcnt(0)
	v_sub_u32_e32 v120, v105, v127
	v_sub_u32_e32 v109, v105, v121
	v_sub_u32_e32 v111, v105, v122
	v_sub_u32_e32 v113, v105, v123
	v_sub_u32_e32 v115, v105, v124
	v_sub_u32_e32 v117, v105, v125
	v_sub_u32_e32 v119, v105, v126
	v_med3_i32 v120, v120, 0, v215
	v_med3_i32 v107, v107, 0, v215
	v_med3_i32 v109, v109, 0, v215
	v_med3_i32 v111, v111, 0, v215
	v_med3_i32 v113, v113, 0, v215
	v_med3_i32 v115, v115, 0, v215
	v_med3_i32 v117, v117, 0, v215
	v_med3_i32 v119, v119, 0, v215
	v_lshl_add_u32 v124, v120, 2, s1
	v_lshl_add_u32 v107, v107, 2, s1
	v_lshl_add_u32 v109, v109, 2, s1
	v_lshl_add_u32 v111, v111, 2, s1
	v_lshl_add_u32 v113, v113, 2, s1
	v_lshl_add_u32 v115, v115, 2, s1
	v_lshl_add_u32 v117, v117, 2, s1
	v_lshl_add_u32 v119, v119, 2, s1
	ds_read_b128 v[120:123], v131 offset:64
	ds_read_b32 v128, v107
	ds_read_b32 v129, v109
	ds_read_b32 v132, v111
	ds_read_b32 v133, v113
	ds_read_b32 v134, v115
	ds_read_b32 v135, v117
	ds_read_b32 v136, v119
	ds_read_b32 v137, v124
	ds_read_b128 v[124:127], v131 offset:96
	s_waitcnt lgkmcnt(9)
	v_sub_u32_e32 v107, v105, v120
	v_sub_u32_e32 v109, v105, v121
	v_med3_i32 v107, v107, 0, v215
	v_med3_i32 v109, v109, 0, v215
	v_sub_u32_e32 v111, v105, v122
	v_sub_u32_e32 v113, v105, v123
	s_waitcnt lgkmcnt(0)
	v_sub_u32_e32 v115, v105, v124
	v_sub_u32_e32 v117, v105, v125
	v_sub_u32_e32 v119, v105, v126
	v_sub_u32_e32 v120, v105, v127
	v_lshl_add_u32 v107, v107, 2, s1
	v_lshl_add_u32 v109, v109, 2, s1
	v_med3_i32 v111, v111, 0, v215
	v_med3_i32 v113, v113, 0, v215
	v_med3_i32 v115, v115, 0, v215
	v_med3_i32 v117, v117, 0, v215
	v_med3_i32 v119, v119, 0, v215
	v_med3_i32 v120, v120, 0, v215
	v_pk_fma_f32 v[66:67], v[66:67], s[14:15], v[128:129] op_sel_hi:[1,0,1]
	v_lshl_add_u32 v111, v111, 2, s1
	v_lshl_add_u32 v113, v113, 2, s1
	v_lshl_add_u32 v115, v115, 2, s1
	v_lshl_add_u32 v117, v117, 2, s1
	v_lshl_add_u32 v119, v119, 2, s1
	v_lshl_add_u32 v120, v120, 2, s1
	ds_read_b32 v122, v107
	ds_read_b32 v123, v109
	ds_read_b32 v124, v111
	ds_read_b32 v125, v113
	ds_read_b32 v138, v115
	ds_read_b32 v139, v117
	ds_read_b32 v140, v119
	ds_read_b32 v141, v120
	v_cndmask_b32_e64 v109, v216, v67, s[44:45]
	v_cndmask_b32_e64 v107, v216, v66, s[46:47]
	v_pk_fma_f32 v[66:67], v[68:69], s[14:15], v[132:133] op_sel_hi:[1,0,1]
	v_max3_f32 v113, v103, v107, v109
	v_cndmask_b32_e64 v111, v216, v67, s[48:49]
	v_cndmask_b32_e64 v115, v216, v66, s[50:51]
	v_pk_fma_f32 v[66:67], v[70:71], s[14:15], v[134:135] op_sel_hi:[1,0,1]
	v_max3_f32 v68, v113, v115, v111
	v_cndmask_b32_e64 v113, v216, v67, s[52:53]
	v_cndmask_b32_e64 v117, v216, v66, s[54:55]
	v_pk_fma_f32 v[66:67], v[72:73], s[14:15], v[136:137] op_sel_hi:[1,0,1]
	v_max3_f32 v68, v68, v117, v113
	v_cndmask_b32_e64 v120, v216, v67, s[56:57]
	v_cndmask_b32_e64 v121, v216, v66, s[58:59]
	s_waitcnt lgkmcnt(6)
	v_pk_fma_f32 v[66:67], v[74:75], s[14:15], v[122:123] op_sel_hi:[1,0,1]
	v_max3_f32 v68, v68, v121, v120
	v_cndmask_b32_e64 v122, v216, v67, s[60:61]
	v_cndmask_b32_e64 v123, v216, v66, s[62:63]
	s_waitcnt lgkmcnt(4)
	v_pk_fma_f32 v[66:67], v[76:77], s[14:15], v[124:125] op_sel_hi:[1,0,1]
	v_max3_f32 v68, v68, v123, v122
	v_cndmask_b32_e64 v124, v216, v67, s[64:65]
	v_cndmask_b32_e64 v126, v216, v66, s[66:67]
	s_waitcnt lgkmcnt(2)
	v_pk_fma_f32 v[66:67], v[78:79], s[14:15], v[138:139] op_sel_hi:[1,0,1]
	v_max3_f32 v68, v68, v126, v124
	v_cndmask_b32_e64 v125, v216, v67, s[68:69]
	v_cndmask_b32_e64 v127, v216, v66, s[70:71]
	s_waitcnt lgkmcnt(0)
	v_pk_fma_f32 v[66:67], v[80:81], s[14:15], v[140:141] op_sel_hi:[1,0,1]
	v_max3_f32 v68, v68, v127, v125
	v_cndmask_b32_e64 v128, v216, v67, s[72:73]
	v_cndmask_b32_e64 v129, v216, v66, s[74:75]
	v_max3_f32 v130, v68, v129, v128

.LBB0_2148:
	v_readlane_b32 s2, v249, 15
	v_readlane_b32 s3, v249, 16
	s_cmp_lt_i32 s2, 42
	s_cselect_b64 s[0:1], -1, 0
	s_cmp_gt_i32 s3, 41
	s_cselect_b64 s[2:3], -1, 0
	s_and_b64 s[0:1], s[0:1], s[2:3]
	s_and_b64 vcc, exec, s[0:1]
	v_readlane_b32 s14, v250, 3
	v_readlane_b32 s15, v250, 4
	s_cbranch_vccz .LBB0_2154
	s_nop 0
	v_readfirstlane_b32 s0, v0
	s_ashr_i32 s2, s0, 6
	v_readlane_b32 s0, v249, 4
	s_lshl_b32 s3, s0, 3
	s_add_i32 s10, s2, s3
	s_cmp_gt_i32 s10, 0xffff
	s_cbranch_scc1 .LBB0_2154
	v_and_b32_e32 v1, 63, v0
	v_xor_b32_e32 v2, 1, v1
	v_xor_b32_e32 v3, 2, v1
	v_xor_b32_e32 v4, 4, v1
	v_xor_b32_e32 v5, 8, v1
	v_xor_b32_e32 v6, 16, v1
	v_xor_b32_e32 v7, 32, v1
	v_lshlrev_b32_e32 v2, 2, v2
	v_lshlrev_b32_e32 v3, 2, v3
	v_lshlrev_b32_e32 v4, 2, v4
	v_lshlrev_b32_e32 v5, 2, v5
	v_lshlrev_b32_e32 v6, 2, v6
	v_lshlrev_b32_e32 v7, 2, v7
	v_lshlrev_b32_e32 v8, 2, v1
	v_lshlrev_b32_e32 v9, 3, v1
	v_lshlrev_b32_e32 v10, 4, v1
	v_cmp_gt_u32_e64 s[30:31], 16, v1
	v_readlane_b32 s16, v249, 5
	v_readlane_b32 s17, v249, 6
	v_readlane_b32 s18, v249, 11
	v_readlane_b32 s19, v249, 12
	v_readlane_b32 s28, v249, 13
	v_readlane_b32 s29, v249, 14
	v_mov_b32_e32 v58, 0x358637bd
	v_mov_b32_e32 v59, 0x260
	s_mov_b32 s11, 0xf800000
	s_add_u32 s20, s16, 0x15f00000
	s_addc_u32 s21, s17, 0
	s_add_u32 s26, s16, 0xdf00000
	s_addc_u32 s27, s17, 0
	s_mov_b32 s33, 0
	s_lshl_b32 s15, s14, 1
	global_load_dwordx4 v[12:15], v10, s[18:19]
	global_load_dwordx4 v[16:19], v10, s[18:19] offset:1024
	global_load_dwordx4 v[20:23], v10, s[18:19] offset:2048
	global_load_dwordx4 v[24:27], v10, s[18:19] offset:3072
	s_mov_b32 s42, s10
	s_add_i32 s43, s10, s14
	s_min_i32 s32, s42, 0xffff
	s_lshl_b64 s[34:35], s[32:33], 6
	s_add_u32 s34, s34, s20
	s_addc_u32 s35, s35, s21
	s_lshl_b64 s[36:37], s[32:33], 11
	s_add_u32 s36, s36, s26
	s_addc_u32 s37, s37, s27
	v_mov_b32_e32 v28, 0
	s_mov_b64 s[38:39], exec
	s_mov_b64 exec, s[30:31]
	global_load_dword v28, v8, s[34:35]
	s_mov_b64 exec, s[38:39]
	global_load_dwordx2 v[30:31], v9, s[36:37]
	global_load_dwordx2 v[32:33], v9, s[36:37] offset:512
	global_load_dwordx2 v[34:35], v9, s[36:37] offset:1024
	global_load_dwordx2 v[36:37], v9, s[36:37] offset:1536
	s_min_i32 s32, s43, 0xffff
	s_lshl_b64 s[34:35], s[32:33], 6
	s_add_u32 s34, s34, s20
	s_addc_u32 s35, s35, s21
	s_lshl_b64 s[36:37], s[32:33], 11
	s_add_u32 s36, s36, s26
	s_addc_u32 s37, s37, s27
	v_mov_b32_e32 v29, 0
	s_mov_b64 s[38:39], exec
	s_mov_b64 exec, s[30:31]
	global_load_dword v29, v8, s[34:35]
	s_mov_b64 exec, s[38:39]
	global_load_dwordx2 v[38:39], v9, s[36:37]
	global_load_dwordx2 v[40:41], v9, s[36:37] offset:512
	global_load_dwordx2 v[42:43], v9, s[36:37] offset:1024
	global_load_dwordx2 v[44:45], v9, s[36:37] offset:1536
	s_waitcnt vmcnt(5)
	s_branch .Lfin_procA
.Lfin_loop:
	s_waitcnt vmcnt(9)
.Lfin_procA:
	s_cmp_gt_i32 s42, 0xffff
	s_cbranch_scc1 .LBB0_2154
	ds_bpermute_b32 v46, v2, v28
	s_waitcnt lgkmcnt(0)
	v_add_f32_e32 v28, v28, v46
	ds_bpermute_b32 v46, v3, v28
	s_waitcnt lgkmcnt(0)
	v_add_f32_e32 v28, v28, v46
	ds_bpermute_b32 v46, v4, v28
	s_waitcnt lgkmcnt(0)
	v_add_f32_e32 v28, v28, v46
	ds_bpermute_b32 v46, v5, v28
	s_waitcnt lgkmcnt(0)
	v_add_f32_e32 v28, v28, v46
	ds_bpermute_b32 v46, v6, v28
	s_waitcnt lgkmcnt(0)
	v_add_f32_e32 v28, v28, v46
	ds_bpermute_b32 v46, v7, v28
	s_waitcnt lgkmcnt(0)
	v_add_f32_e32 v28, v28, v46
	v_fmamk_f32 v48, v28, 0x3a800000, v58
	v_mul_f32_e32 v49, 0x4f800000, v48
	v_cmp_gt_f32_e32 vcc, s11, v48
	s_nop 1
	v_cndmask_b32_e32 v48, v48, v49, vcc
	v_sqrt_f32_e32 v49, v48
	s_nop 0
	v_add_u32_e32 v50, -1, v49
	v_add_u32_e32 v51, 1, v49
	v_fma_f32 v52, -v50, v49, v48
	v_fma_f32 v53, -v51, v49, v48
	v_cmp_ge_f32_e64 s[2:3], 0, v52
	s_nop 1
	v_cndmask_b32_e64 v49, v49, v50, s[2:3]
	v_cmp_lt_f32_e64 s[2:3], 0, v53
	s_nop 1
	v_cndmask_b32_e64 v49, v49, v51, s[2:3]
	v_mul_f32_e32 v50, 0x37800000, v49
	v_cndmask_b32_e32 v49, v49, v50, vcc
	v_cmp_class_f32_e32 vcc, v48, v59
	s_nop 1
	v_cndmask_b32_e32 v48, v49, v48, vcc
	v_div_scale_f32 v49, s[2:3], v48, v48, 1.0
	v_rcp_f32_e32 v50, v49
	v_div_scale_f32 v51, vcc, 1.0, v48, 1.0
	v_fma_f32 v52, -v49, v50, 1.0
	v_fmac_f32_e32 v50, v52, v50
	v_mul_f32_e32 v52, v51, v50
	v_fma_f32 v53, -v49, v52, v51
	v_fmac_f32_e32 v52, v53, v50
	v_fma_f32 v49, -v49, v52, v51
	v_div_fmas_f32 v49, v49, v50, v52
	v_div_fixup_f32 v56, v49, v48, 1.0
	s_mov_b32 s32, s42
	s_lshl_b64 s[40:41], s[32:33], 12
	s_add_u32 s40, s40, s28
	s_addc_u32 s41, s41, s29
	v_lshlrev_b32_e32 v60, 16, v30
	v_and_b32_e32 v61, 0xffff0000, v30
	v_lshlrev_b32_e32 v62, 16, v31
	v_and_b32_e32 v63, 0xffff0000, v31
	v_pk_mul_f32 v[60:61], v[56:57], v[60:61] op_sel_hi:[0,1]
	v_pk_mul_f32 v[62:63], v[56:57], v[62:63] op_sel_hi:[0,1]
	v_pk_mul_f32 v[64:65], v[12:13], v[60:61]
	v_pk_mul_f32 v[66:67], v[14:15], v[62:63]
	global_store_dwordx4 v10, v[64:67], s[40:41]
	s_nop 1
	v_lshlrev_b32_e32 v60, 16, v32
	v_and_b32_e32 v61, 0xffff0000, v32
	v_lshlrev_b32_e32 v62, 16, v33
	v_and_b32_e32 v63, 0xffff0000, v33
	v_pk_mul_f32 v[60:61], v[56:57], v[60:61] op_sel_hi:[0,1]
	v_pk_mul_f32 v[62:63], v[56:57], v[62:63] op_sel_hi:[0,1]
	v_pk_mul_f32 v[64:65], v[16:17], v[60:61]
	v_pk_mul_f32 v[66:67], v[18:19], v[62:63]
	global_store_dwordx4 v10, v[64:67], s[40:41] offset:1024
	s_nop 1
	v_lshlrev_b32_e32 v60, 16, v34
	v_and_b32_e32 v61, 0xffff0000, v34
	v_lshlrev_b32_e32 v62, 16, v35
	v_and_b32_e32 v63, 0xffff0000, v35
	v_pk_mul_f32 v[60:61], v[56:57], v[60:61] op_sel_hi:[0,1]
	v_pk_mul_f32 v[62:63], v[56:57], v[62:63] op_sel_hi:[0,1]
	v_pk_mul_f32 v[64:65], v[20:21], v[60:61]
	v_pk_mul_f32 v[66:67], v[22:23], v[62:63]
	global_store_dwordx4 v10, v[64:67], s[40:41] offset:2048
	s_nop 1
	v_lshlrev_b32_e32 v60, 16, v36
	v_and_b32_e32 v61, 0xffff0000, v36
	v_lshlrev_b32_e32 v62, 16, v37
	v_and_b32_e32 v63, 0xffff0000, v37
	v_pk_mul_f32 v[60:61], v[56:57], v[60:61] op_sel_hi:[0,1]
	v_pk_mul_f32 v[62:63], v[56:57], v[62:63] op_sel_hi:[0,1]
	v_pk_mul_f32 v[64:65], v[24:25], v[60:61]
	v_pk_mul_f32 v[66:67], v[26:27], v[62:63]
	global_store_dwordx4 v10, v[64:67], s[40:41] offset:3072
	s_add_i32 s42, s42, s15
	s_min_i32 s32, s42, 0xffff
	s_lshl_b64 s[34:35], s[32:33], 6
	s_add_u32 s34, s34, s20
	s_addc_u32 s35, s35, s21
	s_lshl_b64 s[36:37], s[32:33], 11
	s_add_u32 s36, s36, s26
	s_addc_u32 s37, s37, s27
	v_mov_b32_e32 v28, 0
	s_mov_b64 s[38:39], exec
	s_mov_b64 exec, s[30:31]
	global_load_dword v28, v8, s[34:35]
	s_mov_b64 exec, s[38:39]
	global_load_dwordx2 v[30:31], v9, s[36:37]
	global_load_dwordx2 v[32:33], v9, s[36:37] offset:512
	global_load_dwordx2 v[34:35], v9, s[36:37] offset:1024
	global_load_dwordx2 v[36:37], v9, s[36:37] offset:1536
	s_waitcnt vmcnt(9)
	s_cmp_gt_i32 s43, 0xffff
	s_cbranch_scc1 .LBB0_2154
	ds_bpermute_b32 v46, v2, v29
	s_waitcnt lgkmcnt(0)
	v_add_f32_e32 v29, v29, v46
	ds_bpermute_b32 v46, v3, v29
	s_waitcnt lgkmcnt(0)
	v_add_f32_e32 v29, v29, v46
	ds_bpermute_b32 v46, v4, v29
	s_waitcnt lgkmcnt(0)
	v_add_f32_e32 v29, v29, v46
	ds_bpermute_b32 v46, v5, v29
	s_waitcnt lgkmcnt(0)
	v_add_f32_e32 v29, v29, v46
	ds_bpermute_b32 v46, v6, v29
	s_waitcnt lgkmcnt(0)
	v_add_f32_e32 v29, v29, v46
	ds_bpermute_b32 v46, v7, v29
	s_waitcnt lgkmcnt(0)
	v_add_f32_e32 v29, v29, v46
	v_fmamk_f32 v48, v29, 0x3a800000, v58
	v_mul_f32_e32 v49, 0x4f800000, v48
	v_cmp_gt_f32_e32 vcc, s11, v48
	s_nop 1
	v_cndmask_b32_e32 v48, v48, v49, vcc
	v_sqrt_f32_e32 v49, v48
	s_nop 0
	v_add_u32_e32 v50, -1, v49
	v_add_u32_e32 v51, 1, v49
	v_fma_f32 v52, -v50, v49, v48
	v_fma_f32 v53, -v51, v49, v48
	v_cmp_ge_f32_e64 s[2:3], 0, v52
	s_nop 1
	v_cndmask_b32_e64 v49, v49, v50, s[2:3]
	v_cmp_lt_f32_e64 s[2:3], 0, v53
	s_nop 1
	v_cndmask_b32_e64 v49, v49, v51, s[2:3]
	v_mul_f32_e32 v50, 0x37800000, v49
	v_cndmask_b32_e32 v49, v49, v50, vcc
	v_cmp_class_f32_e32 vcc, v48, v59
	s_nop 1
	v_cndmask_b32_e32 v48, v49, v48, vcc
	v_div_scale_f32 v49, s[2:3], v48, v48, 1.0
	v_rcp_f32_e32 v50, v49
	v_div_scale_f32 v51, vcc, 1.0, v48, 1.0
	v_fma_f32 v52, -v49, v50, 1.0
	v_fmac_f32_e32 v50, v52, v50
	v_mul_f32_e32 v52, v51, v50
	v_fma_f32 v53, -v49, v52, v51
	v_fmac_f32_e32 v52, v53, v50
	v_fma_f32 v49, -v49, v52, v51
	v_div_fmas_f32 v49, v49, v50, v52
	v_div_fixup_f32 v56, v49, v48, 1.0
	s_mov_b32 s32, s43
	s_lshl_b64 s[40:41], s[32:33], 12
	s_add_u32 s40, s40, s28
	s_addc_u32 s41, s41, s29
	v_lshlrev_b32_e32 v60, 16, v38
	v_and_b32_e32 v61, 0xffff0000, v38
	v_lshlrev_b32_e32 v62, 16, v39
	v_and_b32_e32 v63, 0xffff0000, v39
	v_pk_mul_f32 v[60:61], v[56:57], v[60:61] op_sel_hi:[0,1]
	v_pk_mul_f32 v[62:63], v[56:57], v[62:63] op_sel_hi:[0,1]
	v_pk_mul_f32 v[64:65], v[12:13], v[60:61]
	v_pk_mul_f32 v[66:67], v[14:15], v[62:63]
	global_store_dwordx4 v10, v[64:67], s[40:41]
	s_nop 1
	v_lshlrev_b32_e32 v60, 16, v40
	v_and_b32_e32 v61, 0xffff0000, v40
	v_lshlrev_b32_e32 v62, 16, v41
	v_and_b32_e32 v63, 0xffff0000, v41
	v_pk_mul_f32 v[60:61], v[56:57], v[60:61] op_sel_hi:[0,1]
	v_pk_mul_f32 v[62:63], v[56:57], v[62:63] op_sel_hi:[0,1]
	v_pk_mul_f32 v[64:65], v[16:17], v[60:61]
	v_pk_mul_f32 v[66:67], v[18:19], v[62:63]
	global_store_dwordx4 v10, v[64:67], s[40:41] offset:1024
	s_nop 1
	v_lshlrev_b32_e32 v60, 16, v42
	v_and_b32_e32 v61, 0xffff0000, v42
	v_lshlrev_b32_e32 v62, 16, v43
	v_and_b32_e32 v63, 0xffff0000, v43
	v_pk_mul_f32 v[60:61], v[56:57], v[60:61] op_sel_hi:[0,1]
	v_pk_mul_f32 v[62:63], v[56:57], v[62:63] op_sel_hi:[0,1]
	v_pk_mul_f32 v[64:65], v[20:21], v[60:61]
	v_pk_mul_f32 v[66:67], v[22:23], v[62:63]
	global_store_dwordx4 v10, v[64:67], s[40:41] offset:2048
	s_nop 1
	v_lshlrev_b32_e32 v60, 16, v44
	v_and_b32_e32 v61, 0xffff0000, v44
	v_lshlrev_b32_e32 v62, 16, v45
	v_and_b32_e32 v63, 0xffff0000, v45
	v_pk_mul_f32 v[60:61], v[56:57], v[60:61] op_sel_hi:[0,1]
	v_pk_mul_f32 v[62:63], v[56:57], v[62:63] op_sel_hi:[0,1]
	v_pk_mul_f32 v[64:65], v[24:25], v[60:61]
	v_pk_mul_f32 v[66:67], v[26:27], v[62:63]
	global_store_dwordx4 v10, v[64:67], s[40:41] offset:3072
	s_add_i32 s43, s43, s15
	s_min_i32 s32, s43, 0xffff
	s_lshl_b64 s[34:35], s[32:33], 6
	s_add_u32 s34, s34, s20
	s_addc_u32 s35, s35, s21
	s_lshl_b64 s[36:37], s[32:33], 11
	s_add_u32 s36, s36, s26
	s_addc_u32 s37, s37, s27
	v_mov_b32_e32 v29, 0
	s_mov_b64 s[38:39], exec
	s_mov_b64 exec, s[30:31]
	global_load_dword v29, v8, s[34:35]
	s_mov_b64 exec, s[38:39]
	global_load_dwordx2 v[38:39], v9, s[36:37]
	global_load_dwordx2 v[40:41], v9, s[36:37] offset:512
	global_load_dwordx2 v[42:43], v9, s[36:37] offset:1024
	global_load_dwordx2 v[44:45], v9, s[36:37] offset:1536
	s_branch .Lfin_loop

	.amdhsa_kernel _Z8yoco_fwd4Args
		.amdhsa_group_segment_fixed_size 0
		.amdhsa_private_segment_fixed_size 0
		.amdhsa_kernarg_size 496
		.amdhsa_user_sgpr_count 2
		.amdhsa_user_sgpr_dispatch_ptr 0
		.amdhsa_user_sgpr_queue_ptr 0
		.amdhsa_user_sgpr_kernarg_segment_ptr 1
		.amdhsa_user_sgpr_dispatch_id 0
		.amdhsa_user_sgpr_kernarg_preload_length 0
		.amdhsa_user_sgpr_kernarg_preload_offset 0
		.amdhsa_user_sgpr_private_segment_size 0
		.amdhsa_uses_dynamic_stack 0
		.amdhsa_enable_private_segment 0
		.amdhsa_system_sgpr_workgroup_id_x 1
		.amdhsa_system_sgpr_workgroup_id_y 0
		.amdhsa_system_sgpr_workgroup_id_z 0
		.amdhsa_system_sgpr_workgroup_info 0
		.amdhsa_system_vgpr_workitem_id 0
		.amdhsa_next_free_vgpr 256
		.amdhsa_next_free_sgpr 100
		.amdhsa_accum_offset 256
		.amdhsa_reserve_vcc 1
		.amdhsa_float_round_mode_32 0
		.amdhsa_float_round_mode_16_64 0
		.amdhsa_float_denorm_mode_32 3
		.amdhsa_float_denorm_mode_16_64 3
		.amdhsa_dx10_clamp 1
		.amdhsa_ieee_mode 1
		.amdhsa_fp16_overflow 0
		.amdhsa_tg_split 0
		.amdhsa_exception_fp_ieee_invalid_op 0
		.amdhsa_exception_fp_denorm_src 0
		.amdhsa_exception_fp_ieee_div_zero 0
		.amdhsa_exception_fp_ieee_overflow 0
		.amdhsa_exception_fp_ieee_underflow 0
		.amdhsa_exception_fp_ieee_inexact 0
		.amdhsa_exception_int_div_zero 0
	.end_amdhsa_kernel

amdhsa.kernels:
  - .agpr_count:     0
    .args:
      - .offset:         0
        .size:           240
        .value_kind:     by_value
      - .offset:         240
        .size:           4
        .value_kind:     hidden_block_count_x
      - .offset:         244
        .size:           4
        .value_kind:     hidden_block_count_y
      - .offset:         248
        .size:           4
        .value_kind:     hidden_block_count_z
      - .offset:         252
        .size:           2
        .value_kind:     hidden_group_size_x
      - .offset:         254
        .size:           2
        .value_kind:     hidden_group_size_y
      - .offset:         256
        .size:           2
        .value_kind:     hidden_group_size_z
      - .offset:         258
        .size:           2
        .value_kind:     hidden_remainder_x
      - .offset:         260
        .size:           2
        .value_kind:     hidden_remainder_y
      - .offset:         262
        .size:           2
        .value_kind:     hidden_remainder_z
      - .offset:         280
        .size:           8
        .value_kind:     hidden_global_offset_x
      - .offset:         288
        .size:           8
        .value_kind:     hidden_global_offset_y
      - .offset:         296
        .size:           8
        .value_kind:     hidden_global_offset_z
      - .offset:         304
        .size:           2
        .value_kind:     hidden_grid_dims
      - .offset:         360
        .size:           4
        .value_kind:     hidden_dynamic_lds_size
    .group_segment_fixed_size: 0
    .kernarg_segment_align: 8
    .kernarg_segment_size: 496
    .language:       OpenCL C
    .language_version:
      - 2
      - 0
    .max_flat_workgroup_size: 512
    .name:           _Z8yoco_fwd4Args
    .private_segment_fixed_size: 0
    .sgpr_count:     106
    .sgpr_spill_count: 448
    .symbol:         _Z8yoco_fwd4Args.kd
    .uniform_work_group_size: 1
    .uses_dynamic_stack: false
    .vgpr_count:     256
    .vgpr_spill_count: 0
    .wavefront_size: 64
